# speedup vs baseline: 1.0029x; 1.0000x over previous
.Lk4_st4_7:
	v_add_u32_e32 v169, s17, v118
	s_nop 1
	v_readfirstlane_b32 s14, v169
	s_mov_b32 m0, s14
	s_nop 0
	global_load_lds_dwordx4 v[102:103], off nt
	v_add_u32_e32 v169, s17, v90
	s_nop 1
	v_readfirstlane_b32 s14, v169
	s_mov_b32 m0, s14
	s_nop 0
	global_load_lds_dwordx4 v[104:105], off nt
	v_add_u32_e32 v169, s17, v91
	s_nop 1
	v_readfirstlane_b32 s14, v169
	s_mov_b32 m0, s14
	s_nop 0
	global_load_lds_dwordx4 v[108:109], off nt
	v_add_u32_e32 v169, s17, v119
	s_nop 1
	v_readfirstlane_b32 s14, v169
	s_mov_b32 m0, s14
	s_nop 0
	global_load_lds_dwordx4 v[112:113], off nt
	s_add_u32 s52, s10, 0xc00000
	s_addc_u32 s53, s11, 0
	v_lshlrev_b32_e32 v169, 2, v98
	v_lshlrev_b32_e32 v170, 2, v100
	global_load_dwordx4 v[140:143], v169, s[52:53] nt
	global_load_dwordx4 v[144:147], v170, s[52:53] nt
	v_mfma_f32_16x16x32_f16 a[0:3], v[70:73], v[82:85], a[0:3]
	ds_read_b128 v[14:17], v152
	v_mfma_f32_16x16x32_f16 a[4:7], v[70:73], v[86:89], a[4:7]
	ds_read_b128 v[18:21], v154
	v_mfma_f32_16x16x32_f16 a[12:15], v[66:69], v[82:85], a[12:15]
	ds_read_b128 v[42:45], v164
	v_mfma_f32_16x16x32_f16 a[16:19], v[66:69], v[86:89], a[16:19]
	ds_read_b128 v[38:41], v164 offset:1024
	v_mfma_f32_16x16x32_f16 a[28:31], v[58:61], v[82:85], a[28:31]
	ds_read_b128 v[34:37], v164 offset:2048
	v_mfma_f32_16x16x32_f16 a[60:63], v[58:61], v[86:89], a[60:63]
	ds_read_b128 v[30:33], v164 offset:3072
	v_mfma_f32_16x16x32_f16 a[8:11], v[54:57], v[82:85], a[8:11]
	ds_read_b128 v[26:29], v164 offset:4096
	v_mfma_f32_16x16x32_f16 a[20:23], v[54:57], v[86:89], a[20:23]
	ds_read_b128 v[22:25], v164 offset:5120
	v_mfma_f32_16x16x32_f16 a[24:27], v[46:49], v[82:85], a[24:27]
	ds_read_b128 v[10:13], v164 offset:6144
	v_mfma_f32_16x16x32_f16 a[36:39], v[46:49], v[86:89], a[36:39]
	ds_read_b128 v[6:9], v164 offset:7168
	v_mfma_f32_16x16x32_f16 a[44:47], v[50:53], v[82:85], a[44:47]
	ds_read_b128 v[2:5], v164 offset:8192
	v_mfma_f32_16x16x32_f16 a[64:67], v[50:53], v[86:89], a[64:67]
	v_mfma_f32_16x16x32_f16 a[32:35], v[62:65], v[82:85], a[32:35]
	v_mfma_f32_16x16x32_f16 a[40:43], v[62:65], v[86:89], a[40:43]
	v_mfma_f32_16x16x32_f16 a[48:51], v[74:77], v[82:85], a[48:51]
	v_mfma_f32_16x16x32_f16 a[52:55], v[74:77], v[86:89], a[52:55]
	v_mfma_f32_16x16x32_f16 a[56:59], v[78:81], v[82:85], a[56:59]
	v_mfma_f32_16x16x32_f16 a[68:71], v[78:81], v[86:89], a[68:71]
	s_waitcnt lgkmcnt(8)
	v_mfma_f32_16x16x32_f16 a[0:3], v[42:45], v[14:17], a[0:3]
	ds_read_b128 v[82:85], v153
	v_mfma_f32_16x16x32_f16 a[4:7], v[42:45], v[18:21], a[4:7]
	ds_read_b128 v[86:89], v155
	s_waitcnt lgkmcnt(9)
	v_mfma_f32_16x16x32_f16 a[12:15], v[38:41], v[14:17], a[12:15]
	ds_read_b128 v[70:73], v164 offset:9216
	v_mfma_f32_16x16x32_f16 a[16:19], v[38:41], v[18:21], a[16:19]
	ds_read_b128 v[66:69], v164 offset:10240
	s_waitcnt lgkmcnt(10)
	v_mfma_f32_16x16x32_f16 a[28:31], v[34:37], v[14:17], a[28:31]
	ds_read_b128 v[58:61], v164 offset:11264
	v_mfma_f32_16x16x32_f16 a[60:63], v[34:37], v[18:21], a[60:63]
	ds_read_b128 v[54:57], v164 offset:12288
	s_waitcnt lgkmcnt(11)
	v_mfma_f32_16x16x32_f16 a[8:11], v[30:33], v[14:17], a[8:11]
	ds_read_b128 v[46:49], v164 offset:13312
	v_mfma_f32_16x16x32_f16 a[20:23], v[30:33], v[18:21], a[20:23]
	ds_read_b128 v[50:53], v164 offset:14336
	s_waitcnt lgkmcnt(12)
	v_mfma_f32_16x16x32_f16 a[24:27], v[26:29], v[14:17], a[24:27]
	ds_read_b128 v[62:65], v164 offset:15360
	v_mfma_f32_16x16x32_f16 a[36:39], v[26:29], v[18:21], a[36:39]
	ds_read_b128 v[74:77], v164 offset:16384
	s_waitcnt lgkmcnt(13)
	v_mfma_f32_16x16x32_f16 a[44:47], v[22:25], v[14:17], a[44:47]
	ds_read_b128 v[78:81], v164 offset:17408
	v_mfma_f32_16x16x32_f16 a[64:67], v[22:25], v[18:21], a[64:67]
	s_waitcnt lgkmcnt(13)
	v_mfma_f32_16x16x32_f16 a[32:35], v[10:13], v[14:17], a[32:35]
	v_mfma_f32_16x16x32_f16 a[40:43], v[10:13], v[18:21], a[40:43]
	s_waitcnt lgkmcnt(12)
	v_mfma_f32_16x16x32_f16 a[48:51], v[6:9], v[14:17], a[48:51]
	v_mfma_f32_16x16x32_f16 a[52:55], v[6:9], v[18:21], a[52:55]
	s_waitcnt lgkmcnt(11)
	v_mfma_f32_16x16x32_f16 a[56:59], v[2:5], v[14:17], a[56:59]
	v_mfma_f32_16x16x32_f16 a[68:71], v[2:5], v[18:21], a[68:71]
	s_waitcnt vmcnt(12) lgkmcnt(0)
	s_barrier
	s_add_u32 s52, s50, 0x24000
	s_addc_u32 s53, s51, 0
	s_add_i32 m0, s42, 0xc600
	s_nop 0
	global_load_lds_dwordx4 v137, s[52:53]
	s_add_i32 m0, s43, 0xc600
	s_nop 0
	global_load_lds_dwordx4 v138, s[52:53]
	s_cmp_lt_u32 s42, 0x800
	s_cbranch_scc0 .Lk4_st5_8
	s_add_i32 m0, s44, 0xc600
	s_nop 0
	global_load_lds_dwordx4 v139, s[52:53]
.Lk4_st5_8:
	v_mfma_f32_16x16x32_f16 a[0:3], v[70:73], v[82:85], a[0:3]
	ds_read_b128 v[14:17], v156
	v_mfma_f32_16x16x32_f16 a[4:7], v[70:73], v[86:89], a[4:7]
	ds_read_b128 v[18:21], v158
	v_mfma_f32_16x16x32_f16 a[12:15], v[66:69], v[82:85], a[12:15]
	ds_read_b128 v[42:45], v165
	v_mfma_f32_16x16x32_f16 a[16:19], v[66:69], v[86:89], a[16:19]
	ds_read_b128 v[38:41], v165 offset:1024
	v_mfma_f32_16x16x32_f16 a[28:31], v[58:61], v[82:85], a[28:31]
	ds_read_b128 v[34:37], v165 offset:2048
	v_mfma_f32_16x16x32_f16 a[60:63], v[58:61], v[86:89], a[60:63]
	ds_read_b128 v[30:33], v165 offset:3072
	v_mfma_f32_16x16x32_f16 a[8:11], v[54:57], v[82:85], a[8:11]
	ds_read_b128 v[26:29], v165 offset:4096
	v_mfma_f32_16x16x32_f16 a[20:23], v[54:57], v[86:89], a[20:23]
	ds_read_b128 v[22:25], v165 offset:5120
	v_mfma_f32_16x16x32_f16 a[24:27], v[46:49], v[82:85], a[24:27]
	ds_read_b128 v[10:13], v165 offset:6144
	v_mfma_f32_16x16x32_f16 a[36:39], v[46:49], v[86:89], a[36:39]
	ds_read_b128 v[6:9], v165 offset:7168
	v_mfma_f32_16x16x32_f16 a[44:47], v[50:53], v[82:85], a[44:47]
	ds_read_b128 v[2:5], v165 offset:8192
	v_mfma_f32_16x16x32_f16 a[64:67], v[50:53], v[86:89], a[64:67]
	v_mfma_f32_16x16x32_f16 a[32:35], v[62:65], v[82:85], a[32:35]
	v_mfma_f32_16x16x32_f16 a[40:43], v[62:65], v[86:89], a[40:43]
	v_mfma_f32_16x16x32_f16 a[48:51], v[74:77], v[82:85], a[48:51]
	v_mfma_f32_16x16x32_f16 a[52:55], v[74:77], v[86:89], a[52:55]
	v_mfma_f32_16x16x32_f16 a[56:59], v[78:81], v[82:85], a[56:59]
	v_mfma_f32_16x16x32_f16 a[68:71], v[78:81], v[86:89], a[68:71]
	s_waitcnt lgkmcnt(8)
	v_mfma_f32_16x16x32_f16 a[0:3], v[42:45], v[14:17], a[0:3]
	ds_read_b128 v[82:85], v157
	v_mfma_f32_16x16x32_f16 a[4:7], v[42:45], v[18:21], a[4:7]
	ds_read_b128 v[86:89], v159
	s_waitcnt lgkmcnt(9)
	v_mfma_f32_16x16x32_f16 a[12:15], v[38:41], v[14:17], a[12:15]
	ds_read_b128 v[70:73], v165 offset:9216
	v_mfma_f32_16x16x32_f16 a[16:19], v[38:41], v[18:21], a[16:19]
	ds_read_b128 v[66:69], v165 offset:10240
	s_waitcnt lgkmcnt(10)
	v_mfma_f32_16x16x32_f16 a[28:31], v[34:37], v[14:17], a[28:31]
	ds_read_b128 v[58:61], v165 offset:11264
	v_mfma_f32_16x16x32_f16 a[60:63], v[34:37], v[18:21], a[60:63]
	ds_read_b128 v[54:57], v165 offset:12288
	s_waitcnt lgkmcnt(11)
	v_mfma_f32_16x16x32_f16 a[8:11], v[30:33], v[14:17], a[8:11]
	ds_read_b128 v[46:49], v165 offset:13312
	v_mfma_f32_16x16x32_f16 a[20:23], v[30:33], v[18:21], a[20:23]
	ds_read_b128 v[50:53], v165 offset:14336
	s_waitcnt lgkmcnt(12)
	v_mfma_f32_16x16x32_f16 a[24:27], v[26:29], v[14:17], a[24:27]
	ds_read_b128 v[62:65], v165 offset:15360
	v_mfma_f32_16x16x32_f16 a[36:39], v[26:29], v[18:21], a[36:39]
	ds_read_b128 v[74:77], v165 offset:16384
	s_waitcnt lgkmcnt(13)
	v_mfma_f32_16x16x32_f16 a[44:47], v[22:25], v[14:17], a[44:47]
	ds_read_b128 v[78:81], v165 offset:17408
	v_mfma_f32_16x16x32_f16 a[64:67], v[22:25], v[18:21], a[64:67]
	s_waitcnt lgkmcnt(13)
	v_mfma_f32_16x16x32_f16 a[32:35], v[10:13], v[14:17], a[32:35]
	v_mfma_f32_16x16x32_f16 a[40:43], v[10:13], v[18:21], a[40:43]
	s_waitcnt lgkmcnt(12)
	v_mfma_f32_16x16x32_f16 a[48:51], v[6:9], v[14:17], a[48:51]
	v_mfma_f32_16x16x32_f16 a[52:55], v[6:9], v[18:21], a[52:55]
	s_waitcnt lgkmcnt(11)
	v_mfma_f32_16x16x32_f16 a[56:59], v[2:5], v[14:17], a[56:59]
	v_mfma_f32_16x16x32_f16 a[68:71], v[2:5], v[18:21], a[68:71]
	s_waitcnt vmcnt(8) lgkmcnt(0)
	s_barrier
	s_add_u32 s52, s10, 0x800000
	s_addc_u32 s53, s11, 0
	v_lshlrev_b32_e32 v169, 2, v94
	v_readfirstlane_b32 s14, v118
	s_mov_b32 m0, s14
	s_nop 0
	global_load_lds_dwordx4 v169, s[52:53] nt
	v_lshlrev_b32_e32 v169, 2, v96
	v_readfirstlane_b32 s14, v90
	s_mov_b32 m0, s14
	s_nop 0
	global_load_lds_dwordx4 v169, s[52:53] nt
	v_mfma_f32_16x16x32_f16 a[0:3], v[70:73], v[82:85], a[0:3]
	ds_read_b128 v[14:17], v158
	v_mfma_f32_16x16x32_f16 a[4:7], v[70:73], v[86:89], a[4:7]
	ds_read_b128 v[18:21], v160
	v_mfma_f32_16x16x32_f16 a[12:15], v[66:69], v[82:85], a[12:15]
	ds_read_b128 v[42:45], v168
	v_mfma_f32_16x16x32_f16 a[16:19], v[66:69], v[86:89], a[16:19]
	ds_read_b128 v[38:41], v168 offset:1024
	v_mfma_f32_16x16x32_f16 a[28:31], v[58:61], v[82:85], a[28:31]
	ds_read_b128 v[34:37], v168 offset:2048
	v_mfma_f32_16x16x32_f16 a[60:63], v[58:61], v[86:89], a[60:63]
	ds_read_b128 v[30:33], v168 offset:3072
	v_mfma_f32_16x16x32_f16 a[8:11], v[54:57], v[82:85], a[8:11]
	ds_read_b128 v[26:29], v168 offset:4096
	v_mfma_f32_16x16x32_f16 a[20:23], v[54:57], v[86:89], a[20:23]
	ds_read_b128 v[22:25], v168 offset:5120
	v_mfma_f32_16x16x32_f16 a[24:27], v[46:49], v[82:85], a[24:27]
	ds_read_b128 v[10:13], v168 offset:6144
	v_mfma_f32_16x16x32_f16 a[36:39], v[46:49], v[86:89], a[36:39]
	ds_read_b128 v[6:9], v168 offset:7168
	v_mfma_f32_16x16x32_f16 a[44:47], v[50:53], v[82:85], a[44:47]
	ds_read_b128 v[2:5], v168 offset:8192
	v_mfma_f32_16x16x32_f16 a[64:67], v[50:53], v[86:89], a[64:67]
	v_mfma_f32_16x16x32_f16 a[32:35], v[62:65], v[82:85], a[32:35]
	v_mfma_f32_16x16x32_f16 a[40:43], v[62:65], v[86:89], a[40:43]
	v_mfma_f32_16x16x32_f16 a[48:51], v[74:77], v[82:85], a[48:51]
	v_mfma_f32_16x16x32_f16 a[52:55], v[74:77], v[86:89], a[52:55]
	v_mfma_f32_16x16x32_f16 a[56:59], v[78:81], v[82:85], a[56:59]
	v_mfma_f32_16x16x32_f16 a[68:71], v[78:81], v[86:89], a[68:71]
	s_waitcnt lgkmcnt(8)
	v_mfma_f32_16x16x32_f16 a[0:3], v[42:45], v[14:17], a[0:3]
	ds_read_b128 v[82:85], v159
	v_mfma_f32_16x16x32_f16 a[4:7], v[42:45], v[18:21], a[4:7]
	ds_read_b128 v[86:89], v161
	s_waitcnt lgkmcnt(9)
	v_mfma_f32_16x16x32_f16 a[12:15], v[38:41], v[14:17], a[12:15]
	ds_read_b128 v[70:73], v168 offset:9216
	v_mfma_f32_16x16x32_f16 a[16:19], v[38:41], v[18:21], a[16:19]
	ds_read_b128 v[66:69], v168 offset:10240
	s_waitcnt lgkmcnt(10)
	v_mfma_f32_16x16x32_f16 a[28:31], v[34:37], v[14:17], a[28:31]
	ds_read_b128 v[58:61], v168 offset:11264
	v_mfma_f32_16x16x32_f16 a[60:63], v[34:37], v[18:21], a[60:63]
	ds_read_b128 v[54:57], v168 offset:12288
	s_waitcnt lgkmcnt(11)
	v_mfma_f32_16x16x32_f16 a[8:11], v[30:33], v[14:17], a[8:11]
	ds_read_b128 v[46:49], v168 offset:13312
	v_mfma_f32_16x16x32_f16 a[20:23], v[30:33], v[18:21], a[20:23]
	ds_read_b128 v[50:53], v168 offset:14336
	s_waitcnt lgkmcnt(12)
	v_mfma_f32_16x16x32_f16 a[24:27], v[26:29], v[14:17], a[24:27]
	ds_read_b128 v[62:65], v168 offset:15360
	v_mfma_f32_16x16x32_f16 a[36:39], v[26:29], v[18:21], a[36:39]
	ds_read_b128 v[74:77], v168 offset:16384
	s_waitcnt lgkmcnt(13)
	v_mfma_f32_16x16x32_f16 a[44:47], v[22:25], v[14:17], a[44:47]
	ds_read_b128 v[78:81], v168 offset:17408
	v_mfma_f32_16x16x32_f16 a[64:67], v[22:25], v[18:21], a[64:67]
	s_waitcnt lgkmcnt(13)
	v_mfma_f32_16x16x32_f16 a[32:35], v[10:13], v[14:17], a[32:35]
	v_mfma_f32_16x16x32_f16 a[40:43], v[10:13], v[18:21], a[40:43]
	s_waitcnt lgkmcnt(12)
	v_mfma_f32_16x16x32_f16 a[48:51], v[6:9], v[14:17], a[48:51]
	v_mfma_f32_16x16x32_f16 a[52:55], v[6:9], v[18:21], a[52:55]
	s_waitcnt lgkmcnt(11)
	v_mfma_f32_16x16x32_f16 a[56:59], v[2:5], v[14:17], a[56:59]
	v_mfma_f32_16x16x32_f16 a[68:71], v[2:5], v[18:21], a[68:71]
	s_waitcnt vmcnt(2) lgkmcnt(0)
	s_barrier
	v_add_u32_e32 v169, s16, v118
	s_nop 1
	v_readfirstlane_b32 s14, v169
	s_mov_b32 m0, s14
	s_nop 0
	global_load_lds_dwordx4 v[0:1], off nt
	v_add_u32_e32 v169, s16, v90
	s_nop 1
	v_readfirstlane_b32 s14, v169
	s_mov_b32 m0, s14
	s_nop 0
	global_load_lds_dwordx4 v[106:107], off nt
	v_add_u32_e32 v169, s16, v91
	s_nop 1
	v_readfirstlane_b32 s14, v169
	s_mov_b32 m0, s14
	s_nop 0
	global_load_lds_dwordx4 v[110:111], off nt
	v_add_u32_e32 v169, s16, v119
	s_nop 1
	v_readfirstlane_b32 s14, v169
	s_mov_b32 m0, s14
	s_nop 0
	global_load_lds_dwordx4 v[114:115], off nt
	v_mfma_f32_16x16x32_f16 a[0:3], v[70:73], v[82:85], a[0:3]
	ds_read_b128 v[14:17], v160
	v_mfma_f32_16x16x32_f16 a[4:7], v[70:73], v[86:89], a[4:7]
	ds_read_b128 v[18:21], v162
	v_mfma_f32_16x16x32_f16 a[12:15], v[66:69], v[82:85], a[12:15]
	ds_read_b128 v[42:45], v164
	v_mfma_f32_16x16x32_f16 a[16:19], v[66:69], v[86:89], a[16:19]
	ds_read_b128 v[38:41], v164 offset:1024
	v_mfma_f32_16x16x32_f16 a[28:31], v[58:61], v[82:85], a[28:31]
	ds_read_b128 v[34:37], v164 offset:2048
	v_mfma_f32_16x16x32_f16 a[60:63], v[58:61], v[86:89], a[60:63]
	ds_read_b128 v[30:33], v164 offset:3072
	v_mfma_f32_16x16x32_f16 a[8:11], v[54:57], v[82:85], a[8:11]
	ds_read_b128 v[26:29], v164 offset:4096
	v_mfma_f32_16x16x32_f16 a[20:23], v[54:57], v[86:89], a[20:23]
	ds_read_b128 v[22:25], v164 offset:5120
	v_mfma_f32_16x16x32_f16 a[24:27], v[46:49], v[82:85], a[24:27]
	ds_read_b128 v[10:13], v164 offset:6144
	v_mfma_f32_16x16x32_f16 a[36:39], v[46:49], v[86:89], a[36:39]
	ds_read_b128 v[6:9], v164 offset:7168
	v_mfma_f32_16x16x32_f16 a[44:47], v[50:53], v[82:85], a[44:47]
	ds_read_b128 v[2:5], v164 offset:8192
	v_mfma_f32_16x16x32_f16 a[64:67], v[50:53], v[86:89], a[64:67]
	v_mfma_f32_16x16x32_f16 a[32:35], v[62:65], v[82:85], a[32:35]
	v_mfma_f32_16x16x32_f16 a[40:43], v[62:65], v[86:89], a[40:43]
	v_mfma_f32_16x16x32_f16 a[48:51], v[74:77], v[82:85], a[48:51]
	v_mfma_f32_16x16x32_f16 a[52:55], v[74:77], v[86:89], a[52:55]
	v_mfma_f32_16x16x32_f16 a[56:59], v[78:81], v[82:85], a[56:59]
	v_mfma_f32_16x16x32_f16 a[68:71], v[78:81], v[86:89], a[68:71]
	s_waitcnt lgkmcnt(8)
	v_mfma_f32_16x16x32_f16 a[0:3], v[42:45], v[14:17], a[0:3]
	ds_read_b128 v[82:85], v161
	v_mfma_f32_16x16x32_f16 a[4:7], v[42:45], v[18:21], a[4:7]
	ds_read_b128 v[86:89], v163
	s_waitcnt lgkmcnt(9)
	v_mfma_f32_16x16x32_f16 a[12:15], v[38:41], v[14:17], a[12:15]
	ds_read_b128 v[70:73], v164 offset:9216
	v_mfma_f32_16x16x32_f16 a[16:19], v[38:41], v[18:21], a[16:19]
	ds_read_b128 v[66:69], v164 offset:10240
	s_waitcnt lgkmcnt(10)
	v_mfma_f32_16x16x32_f16 a[28:31], v[34:37], v[14:17], a[28:31]
	ds_read_b128 v[58:61], v164 offset:11264
	v_mfma_f32_16x16x32_f16 a[60:63], v[34:37], v[18:21], a[60:63]
	ds_read_b128 v[54:57], v164 offset:12288
	s_waitcnt lgkmcnt(11)
	v_mfma_f32_16x16x32_f16 a[8:11], v[30:33], v[14:17], a[8:11]
	ds_read_b128 v[46:49], v164 offset:13312
	v_mfma_f32_16x16x32_f16 a[20:23], v[30:33], v[18:21], a[20:23]
	ds_read_b128 v[50:53], v164 offset:14336
	s_waitcnt lgkmcnt(12)
	v_mfma_f32_16x16x32_f16 a[24:27], v[26:29], v[14:17], a[24:27]
	ds_read_b128 v[62:65], v164 offset:15360
	v_mfma_f32_16x16x32_f16 a[36:39], v[26:29], v[18:21], a[36:39]
	ds_read_b128 v[74:77], v164 offset:16384
	s_waitcnt lgkmcnt(13)
	v_mfma_f32_16x16x32_f16 a[44:47], v[22:25], v[14:17], a[44:47]
	ds_read_b128 v[78:81], v164 offset:17408
	v_mfma_f32_16x16x32_f16 a[64:67], v[22:25], v[18:21], a[64:67]
	s_waitcnt lgkmcnt(13)
	v_mfma_f32_16x16x32_f16 a[32:35], v[10:13], v[14:17], a[32:35]
	v_mfma_f32_16x16x32_f16 a[40:43], v[10:13], v[18:21], a[40:43]
	s_waitcnt lgkmcnt(12)
	v_mfma_f32_16x16x32_f16 a[48:51], v[6:9], v[14:17], a[48:51]
	v_mfma_f32_16x16x32_f16 a[52:55], v[6:9], v[18:21], a[52:55]
	s_waitcnt lgkmcnt(11)
	v_mfma_f32_16x16x32_f16 a[56:59], v[2:5], v[14:17], a[56:59]
	v_mfma_f32_16x16x32_f16 a[68:71], v[2:5], v[18:21], a[68:71]
	s_waitcnt lgkmcnt(8)
	v_mfma_f32_16x16x32_f16 a[0:3], v[70:73], v[82:85], a[0:3]
	v_mfma_f32_16x16x32_f16 a[4:7], v[70:73], v[86:89], a[4:7]
	s_waitcnt lgkmcnt(9)
	v_mfma_f32_16x16x32_f16 a[12:15], v[66:69], v[82:85], a[12:15]
	v_mfma_f32_16x16x32_f16 a[16:19], v[66:69], v[86:89], a[16:19]
	s_waitcnt lgkmcnt(10)
	v_mfma_f32_16x16x32_f16 a[28:31], v[58:61], v[82:85], a[28:31]
	v_mfma_f32_16x16x32_f16 a[60:63], v[58:61], v[86:89], a[60:63]
	s_waitcnt lgkmcnt(11)
	v_mfma_f32_16x16x32_f16 a[8:11], v[54:57], v[82:85], a[8:11]
	v_mfma_f32_16x16x32_f16 a[20:23], v[54:57], v[86:89], a[20:23]
	s_waitcnt lgkmcnt(12)
	v_mfma_f32_16x16x32_f16 a[24:27], v[46:49], v[82:85], a[24:27]
	v_mfma_f32_16x16x32_f16 a[36:39], v[46:49], v[86:89], a[36:39]
	s_waitcnt lgkmcnt(13)
	v_mfma_f32_16x16x32_f16 a[44:47], v[50:53], v[82:85], a[44:47]
	v_mfma_f32_16x16x32_f16 a[64:67], v[50:53], v[86:89], a[64:67]
	s_waitcnt lgkmcnt(13)
	v_mfma_f32_16x16x32_f16 a[32:35], v[62:65], v[82:85], a[32:35]
	v_mfma_f32_16x16x32_f16 a[40:43], v[62:65], v[86:89], a[40:43]
	s_waitcnt lgkmcnt(12)
	v_mfma_f32_16x16x32_f16 a[48:51], v[74:77], v[82:85], a[48:51]
	v_mfma_f32_16x16x32_f16 a[52:55], v[74:77], v[86:89], a[52:55]
	s_waitcnt lgkmcnt(11)
	v_mfma_f32_16x16x32_f16 a[56:59], v[78:81], v[82:85], a[56:59]
	v_mfma_f32_16x16x32_f16 a[68:71], v[78:81], v[86:89], a[68:71]
	s_waitcnt lgkmcnt(0)
	s_setprio 0
